# phase-start code prefetch de-duplicated: each workgroup touches only its 4 KiB slice ((wg>>3)&7) of the next 32 KiB, offsets precomputed into a1 at entry
# baseline (speedup 1.0000x reference)
_Z4mega5MArgs:
	v_lshlrev_b32_e32 v250, 6, v0
	s_lshr_b32 s100, s2, 3
	s_and_b32 s100, s100, 7
	s_lshl_b32 s100, s100, 12
	v_lshlrev_b32_e32 v251, 3, v0
	v_add_u32_e32 v251, s100, v251
	v_accvgpr_write_b32 a1, v251
	s_load_dwordx4 s[28:31], s[0:1], 0xe0
	s_load_dword s33, s[0:1], 0xf0
	s_add_u32 s4, s0, 0xf0
	s_addc_u32 s5, s1, 0
	v_lshrrev_b32_e32 v1, 6, v0
	s_nop 1
	v_readfirstlane_b32 s98, v1
	v_and_b32_e32 v1, 63, v0
	v_writelane_b32 v249, s4, 0
	v_cmp_eq_u32_e32 vcc, 0, v1
	s_nop 0
	v_writelane_b32 v249, s5, 1
	s_and_saveexec_b64 s[4:5], vcc
	s_cbranch_execz .LBB0_2
	s_getreg_b32 s3, hwreg(HW_REG_HW_ID, 0, 6)
	s_lshl_b32 s3, s3, 2
	s_and_b32 s3, s3, 0xfc
	s_add_i32 s3, s3, 0
	s_add_i32 s3, s3, 0x25c00
	v_lshrrev_b32_e32 v1, 6, v0
	v_mov_b32_e32 v2, s3
	ds_write_b32 v2, v1

.LBB0_239:
	s_or_b64 exec, exec, s[0:1]
	s_barrier
	v_accvgpr_read_b32 v251, a1
	s_getpc_b64 s[100:101]
	global_load_dword a0, v251, s[100:101]

.LBB0_2396:
	s_or_b64 exec, exec, s[0:1]
	s_barrier
	v_accvgpr_read_b32 v251, a1
	s_getpc_b64 s[100:101]
	v_min_u32_e32 v251, 0x7d00, v251
	global_load_dword a0, v251, s[100:101]

.LBB0_2821:
	s_or_b64 exec, exec, s[0:1]
	s_barrier
	v_accvgpr_read_b32 v251, a1
	s_getpc_b64 s[100:101]
	v_min_u32_e32 v251, 0x2600, v251
	global_load_dword a0, v251, s[100:101]

	.amdhsa_kernel _Z4mega5MArgs
		.amdhsa_group_segment_fixed_size 0
		.amdhsa_private_segment_fixed_size 0
		.amdhsa_kernarg_size 496
		.amdhsa_user_sgpr_count 2
		.amdhsa_user_sgpr_dispatch_ptr 0
		.amdhsa_user_sgpr_queue_ptr 0
		.amdhsa_user_sgpr_kernarg_segment_ptr 1
		.amdhsa_user_sgpr_dispatch_id 0
		.amdhsa_user_sgpr_kernarg_preload_length 0
		.amdhsa_user_sgpr_kernarg_preload_offset 0
		.amdhsa_user_sgpr_private_segment_size 0
		.amdhsa_uses_dynamic_stack 0
		.amdhsa_enable_private_segment 0
		.amdhsa_system_sgpr_workgroup_id_x 1
		.amdhsa_system_sgpr_workgroup_id_y 0
		.amdhsa_system_sgpr_workgroup_id_z 0
		.amdhsa_system_sgpr_workgroup_info 0
		.amdhsa_system_vgpr_workitem_id 0
		.amdhsa_next_free_vgpr 254
		.amdhsa_next_free_sgpr 102
		.amdhsa_accum_offset 252
		.amdhsa_reserve_vcc 1
		.amdhsa_float_round_mode_32 0
		.amdhsa_float_round_mode_16_64 0
		.amdhsa_float_denorm_mode_32 3
		.amdhsa_float_denorm_mode_16_64 3
		.amdhsa_dx10_clamp 1
		.amdhsa_ieee_mode 1
		.amdhsa_fp16_overflow 0
		.amdhsa_tg_split 0
		.amdhsa_exception_fp_ieee_invalid_op 0
		.amdhsa_exception_fp_denorm_src 0
		.amdhsa_exception_fp_ieee_div_zero 0
		.amdhsa_exception_fp_ieee_overflow 0
		.amdhsa_exception_fp_ieee_underflow 0
		.amdhsa_exception_fp_ieee_inexact 0
		.amdhsa_exception_int_div_zero 0
	.end_amdhsa_kernel

amdhsa.kernels:
  - .agpr_count:     2
    .args:
      - .offset:         0
        .size:           240
        .value_kind:     by_value
      - .offset:         240
        .size:           4
        .value_kind:     hidden_block_count_x
      - .offset:         244
        .size:           4
        .value_kind:     hidden_block_count_y
      - .offset:         248
        .size:           4
        .value_kind:     hidden_block_count_z
      - .offset:         252
        .size:           2
        .value_kind:     hidden_group_size_x
      - .offset:         254
        .size:           2
        .value_kind:     hidden_group_size_y
      - .offset:         256
        .size:           2
        .value_kind:     hidden_group_size_z
      - .offset:         258
        .size:           2
        .value_kind:     hidden_remainder_x
      - .offset:         260
        .size:           2
        .value_kind:     hidden_remainder_y
      - .offset:         262
        .size:           2
        .value_kind:     hidden_remainder_z
      - .offset:         280
        .size:           8
        .value_kind:     hidden_global_offset_x
      - .offset:         288
        .size:           8
        .value_kind:     hidden_global_offset_y
      - .offset:         296
        .size:           8
        .value_kind:     hidden_global_offset_z
      - .offset:         304
        .size:           2
        .value_kind:     hidden_grid_dims
      - .offset:         360
        .size:           4
        .value_kind:     hidden_dynamic_lds_size
    .group_segment_fixed_size: 0
    .kernarg_segment_align: 8
    .kernarg_segment_size: 496
    .language:       OpenCL C
    .language_version:
      - 2
      - 0
    .max_flat_workgroup_size: 512
    .name:           _Z4mega5MArgs
    .private_segment_fixed_size: 0
    .sgpr_count:     108
    .sgpr_spill_count: 65
    .symbol:         _Z4mega5MArgs.kd
    .uniform_work_group_size: 1
    .uses_dynamic_stack: false
    .vgpr_count:     252
    .vgpr_spill_count: 0
    .wavefront_size: 64
